# C3 per-step trims: hw bf16 convert instead of bit-trick, log2e folded into log-decay inputs (64 fewer VALU per direction)
# speedup vs baseline: 1.0340x; 1.0064x over previous
; #define LAS __attribute__((address_space(3)))
; __device__ __forceinline__ float kf(float x) { asm volatile("" : "+s"(x)); return x; }
; #define lds lds_hidden(lds0)
; __device__ __forceinline__ void attn_phase(LAS unsigned char* lds, const bf16_t* __restrict__ QA, const bf16_t* __restrict__ KA, const bf16_t* __restrict__ VTA, ...
;     ...
;         for (int blk = 0; blk < 4; ++blk) {
;             const int t0 = half * 4 + blk, qr0 = t0 * 16, qo = qr0 + l15;
;             const size_t tok = (size_t)b * SEQ + qb * 128 + qo;
;             const bf16x8 q0 = q0n, q1 = q1n;
;             if (blk < 3) { const size_t tokn = tok + 16; q0n = *(const bf16x8*)(QA + tokn * 512 + head * 64 + 8 * g4); q1n = *(const bf16x8*)(QA + tokn * 512 + head * 64 + 32 + 8 * g4); }
;             f32x4 sc[18];
;             float mx = sk;
; #pragma unroll
;             for (int i = 0; i < 18; ++i) {
;                 const LAS unsigned char* kp = lds + ((t0 + i) * 16 + l15) * KROW;
;                 const bf16x8 k0 = *(const LAS bf16x8*)(kp + kc0), k1 = *(const LAS bf16x8*)(kp + (kc0 ^ 64));
;                 f32x4 a = (f32x4){0.f, 0.f, 0.f, 0.f};
;                 a = __builtin_amdgcn_mfma_f32_16x16x32_bf16(k0, q0, a, 0, 0, 0);
;                 a = __builtin_amdgcn_mfma_f32_16x16x32_bf16(k1, q1, a, 0, 0, 0);
; #pragma unroll
;                 for (int r = 0; r < 4; ++r) {
;                     const int kap = (t0 + i) * 16 + 4 * g4 + r, rel = kap - qo, kpos = kb0 + kap;
;                     const bool ok = (rel >= 0) && (rel <= 256) && (kpos >= 0) && (kpos < SEQ);
;                     a[r] = ok ? a[r] : kf(-1e30f);
;                     mx = fmaxf(mx, a[r]);
;                 }
;                 sc[i] = a;
;             }
.LBB0_776:
	v_add_u32_e32 v148, s30, v145
	v_add_u32_e32 v149, s30, v146
	ds_read_b128 v[36:39], v148
	ds_read_b128 v[40:43], v149
	ds_read_b128 v[44:47], v148 offset:2048
	ds_read_b128 v[48:51], v149 offset:2048
	ds_read_b128 v[52:55], v148 offset:4096
	ds_read_b128 v[56:59], v149 offset:4096
	v_sub_u32_e32 v150, v129, v88
	v_add_u32_e32 v160, s30, v147
	v_add_u32_e32 v151, 0xc800, v160
	v_add_u32_e32 v152, 0xfb00, v160
	v_add_u32_e32 v153, 0x12e00, v160
	v_add_u32_e32 v154, 0x16100, v160
	s_add_i32 s44, s42, s43
	s_mov_b32 s16, 0x3fb8aa3b
	v_mbcnt_lo_u32_b32 v161, -1, 0
	v_mbcnt_hi_u32_b32 v161, -1, v161
	v_lshlrev_b32_e32 v161, 2, v161
	v_xor_b32_e32 v158, 64, v161
	v_xor_b32_e32 v159, 0x80, v161
	v_mov_b32_e32 v155, v144
	v_mov_b32_e32 v180, 0xf149f2ca
	s_lshr_b32 s17, s42, 7
	s_add_i32 s17, s17, -1
	s_cmp_lt_u32 s17, 14
	s_cbranch_scc1 .Lattn_fast_1
	s_waitcnt lgkmcnt(4)
	v_mfma_f32_16x16x32_bf16 v[182:185], v[36:39], v[14:17], 0
	v_mfma_f32_16x16x32_bf16 v[182:185], v[40:43], v[10:13], v[182:185]
	ds_read_b128 v[60:63], v148 offset:6144
	ds_read_b128 v[64:67], v149 offset:6144
	s_waitcnt lgkmcnt(4)
	v_mfma_f32_16x16x32_bf16 v[186:189], v[44:47], v[14:17], 0
	v_mfma_f32_16x16x32_bf16 v[186:189], v[48:51], v[10:13], v[186:189]
	ds_read_b128 v[36:39], v148 offset:8192
	ds_read_b128 v[40:43], v149 offset:8192
	s_waitcnt lgkmcnt(4)
	v_mfma_f32_16x16x32_bf16 v[190:193], v[52:55], v[14:17], 0
	v_mfma_f32_16x16x32_bf16 v[190:193], v[56:59], v[10:13], v[190:193]
	ds_read_b128 v[44:47], v148 offset:10240
	ds_read_b128 v[48:51], v149 offset:10240
	s_add_i32 s17, s44, -128
	s_cmpk_lt_u32 s17, 0x800
	s_cselect_b64 s[0:1], -1, 0
	v_cmp_le_i32_e32 vcc, 0, v150
	s_and_b64 vcc, vcc, s[0:1]
	v_cndmask_b32_e32 v182, v180, v182, vcc
	v_cmp_le_i32_e32 vcc, -1, v150
	s_and_b64 vcc, vcc, s[0:1]
	v_cndmask_b32_e32 v183, v180, v183, vcc
	v_cmp_le_i32_e32 vcc, -2, v150
	s_and_b64 vcc, vcc, s[0:1]
	v_cndmask_b32_e32 v184, v180, v184, vcc
	v_cmp_le_i32_e32 vcc, -3, v150
	s_and_b64 vcc, vcc, s[0:1]
	v_cndmask_b32_e32 v185, v180, v185, vcc
	v_max3_f32 v155, v155, v182, v183
	v_max3_f32 v155, v155, v184, v185
	s_waitcnt lgkmcnt(4)
	v_mfma_f32_16x16x32_bf16 v[194:197], v[60:63], v[14:17], 0
	v_mfma_f32_16x16x32_bf16 v[194:197], v[64:67], v[10:13], v[194:197]
	ds_read_b128 v[52:55], v148 offset:12288
	ds_read_b128 v[56:59], v149 offset:12288
	s_add_i32 s17, s44, -112
	s_cmpk_lt_u32 s17, 0x800
	s_cselect_b64 vcc, -1, 0
	v_cndmask_b32_e32 v186, v180, v186, vcc
	v_cndmask_b32_e32 v187, v180, v187, vcc
	v_cndmask_b32_e32 v188, v180, v188, vcc
	v_cndmask_b32_e32 v189, v180, v189, vcc
	v_max3_f32 v155, v155, v186, v187
	v_max3_f32 v155, v155, v188, v189
	s_waitcnt lgkmcnt(4)
	v_mfma_f32_16x16x32_bf16 v[198:201], v[36:39], v[14:17], 0
	v_mfma_f32_16x16x32_bf16 v[198:201], v[40:43], v[10:13], v[198:201]
	ds_read_b128 v[60:63], v148 offset:14336
	ds_read_b128 v[64:67], v149 offset:14336
	s_add_i32 s17, s44, -96
	s_cmpk_lt_u32 s17, 0x800
	s_cselect_b64 vcc, -1, 0
	v_cndmask_b32_e32 v190, v180, v190, vcc
	v_cndmask_b32_e32 v191, v180, v191, vcc
	v_cndmask_b32_e32 v192, v180, v192, vcc
	v_cndmask_b32_e32 v193, v180, v193, vcc
	v_max3_f32 v155, v155, v190, v191
	v_max3_f32 v155, v155, v192, v193
	s_waitcnt lgkmcnt(4)
	v_mfma_f32_16x16x32_bf16 v[202:205], v[44:47], v[14:17], 0
	v_mfma_f32_16x16x32_bf16 v[202:205], v[48:51], v[10:13], v[202:205]
	ds_read_b128 v[36:39], v148 offset:16384
	ds_read_b128 v[40:43], v149 offset:16384
	s_add_i32 s17, s44, -80
	s_cmpk_lt_u32 s17, 0x800
	s_cselect_b64 vcc, -1, 0
	v_cndmask_b32_e32 v194, v180, v194, vcc
	v_cndmask_b32_e32 v195, v180, v195, vcc
	v_cndmask_b32_e32 v196, v180, v196, vcc
	v_cndmask_b32_e32 v197, v180, v197, vcc
	v_max3_f32 v155, v155, v194, v195
	v_max3_f32 v155, v155, v196, v197
	s_waitcnt lgkmcnt(4)
	v_mfma_f32_16x16x32_bf16 v[206:209], v[52:55], v[14:17], 0
	v_mfma_f32_16x16x32_bf16 v[206:209], v[56:59], v[10:13], v[206:209]
	ds_read_b128 v[44:47], v148 offset:18432
	ds_read_b128 v[48:51], v149 offset:18432
	s_add_i32 s17, s44, -64
	s_cmpk_lt_u32 s17, 0x800
	s_cselect_b64 vcc, -1, 0
	v_cndmask_b32_e32 v198, v180, v198, vcc
	v_cndmask_b32_e32 v199, v180, v199, vcc
	v_cndmask_b32_e32 v200, v180, v200, vcc
	v_cndmask_b32_e32 v201, v180, v201, vcc
	v_max3_f32 v155, v155, v198, v199
	v_max3_f32 v155, v155, v200, v201
	s_waitcnt lgkmcnt(4)
	v_mfma_f32_16x16x32_bf16 v[210:213], v[60:63], v[14:17], 0
	v_mfma_f32_16x16x32_bf16 v[210:213], v[64:67], v[10:13], v[210:213]
	ds_read_b128 v[52:55], v148 offset:20480
	ds_read_b128 v[56:59], v149 offset:20480
	s_add_i32 s17, s44, -48
	s_cmpk_lt_u32 s17, 0x800
	s_cselect_b64 vcc, -1, 0
	v_cndmask_b32_e32 v202, v180, v202, vcc
	v_cndmask_b32_e32 v203, v180, v203, vcc
	v_cndmask_b32_e32 v204, v180, v204, vcc
	v_cndmask_b32_e32 v205, v180, v205, vcc
	v_max3_f32 v155, v155, v202, v203
	v_max3_f32 v155, v155, v204, v205
	s_waitcnt lgkmcnt(4)
	v_mfma_f32_16x16x32_bf16 v[214:217], v[36:39], v[14:17], 0
	v_mfma_f32_16x16x32_bf16 v[214:217], v[40:43], v[10:13], v[214:217]
	ds_read_b128 v[60:63], v148 offset:22528
	ds_read_b128 v[64:67], v149 offset:22528
	s_add_i32 s17, s44, -32
	s_cmpk_lt_u32 s17, 0x800
	s_cselect_b64 vcc, -1, 0
	v_cndmask_b32_e32 v206, v180, v206, vcc
	v_cndmask_b32_e32 v207, v180, v207, vcc
	v_cndmask_b32_e32 v208, v180, v208, vcc
	v_cndmask_b32_e32 v209, v180, v209, vcc
	v_max3_f32 v155, v155, v206, v207
	v_max3_f32 v155, v155, v208, v209
	s_waitcnt lgkmcnt(4)
; #define LAS __attribute__((address_space(3)))
; __device__ __forceinline__ float kf(float x) { asm volatile("" : "+s"(x)); return x; }
; #define lds lds_hidden(lds0)
; __device__ __forceinline__ void attn_phase(LAS unsigned char* lds, const bf16_t* __restrict__ QA, const bf16_t* __restrict__ KA, const bf16_t* __restrict__ VTA, ...
;     ...
;             for (int i = 0; i < 18; ++i) {
;                 const LAS unsigned char* kp = lds + ((t0 + i) * 16 + l15) * KROW;
;                 const bf16x8 k0 = *(const LAS bf16x8*)(kp + kc0), k1 = *(const LAS bf16x8*)(kp + (kc0 ^ 64));
;                 f32x4 a = (f32x4){0.f, 0.f, 0.f, 0.f};
;                 a = __builtin_amdgcn_mfma_f32_16x16x32_bf16(k0, q0, a, 0, 0, 0);
;                 a = __builtin_amdgcn_mfma_f32_16x16x32_bf16(k1, q1, a, 0, 0, 0);
; #pragma unroll
;                 for (int r = 0; r < 4; ++r) {
;                     const int kap = (t0 + i) * 16 + 4 * g4 + r, rel = kap - qo, kpos = kb0 + kap;
;                     const bool ok = (rel >= 0) && (rel <= 256) && (kpos >= 0) && (kpos < SEQ);
;                     a[r] = ok ? a[r] : kf(-1e30f);
;                     mx = fmaxf(mx, a[r]);
;                 }
;                 sc[i] = a;
;             }
	v_mfma_f32_16x16x32_bf16 v[218:221], v[44:47], v[14:17], 0
	v_mfma_f32_16x16x32_bf16 v[218:221], v[48:51], v[10:13], v[218:221]
	ds_read_b128 v[36:39], v148 offset:24576
	ds_read_b128 v[40:43], v149 offset:24576
	s_add_i32 s17, s44, -16
	s_cmpk_lt_u32 s17, 0x800
	s_cselect_b64 vcc, -1, 0
	v_cndmask_b32_e32 v210, v180, v210, vcc
	v_cndmask_b32_e32 v211, v180, v211, vcc
	v_cndmask_b32_e32 v212, v180, v212, vcc
	v_cndmask_b32_e32 v213, v180, v213, vcc
	v_max3_f32 v155, v155, v210, v211
	v_max3_f32 v155, v155, v212, v213
	s_waitcnt lgkmcnt(4)
	v_mfma_f32_16x16x32_bf16 v[222:225], v[52:55], v[14:17], 0
	v_mfma_f32_16x16x32_bf16 v[222:225], v[56:59], v[10:13], v[222:225]
	ds_read_b128 v[44:47], v148 offset:26624
	ds_read_b128 v[48:51], v149 offset:26624
	s_add_i32 s17, s44, 0
	s_cmpk_lt_u32 s17, 0x800
	s_cselect_b64 vcc, -1, 0
	v_cndmask_b32_e32 v214, v180, v214, vcc
	v_cndmask_b32_e32 v215, v180, v215, vcc
	v_cndmask_b32_e32 v216, v180, v216, vcc
	v_cndmask_b32_e32 v217, v180, v217, vcc
	v_max3_f32 v155, v155, v214, v215
	v_max3_f32 v155, v155, v216, v217
	s_waitcnt lgkmcnt(4)
	v_mfma_f32_16x16x32_bf16 v[226:229], v[60:63], v[14:17], 0
	v_mfma_f32_16x16x32_bf16 v[226:229], v[64:67], v[10:13], v[226:229]
	ds_read_b128 v[52:55], v148 offset:28672
	ds_read_b128 v[56:59], v149 offset:28672
	s_add_i32 s17, s44, 16
	s_cmpk_lt_u32 s17, 0x800
	s_cselect_b64 vcc, -1, 0
	v_cndmask_b32_e32 v218, v180, v218, vcc
	v_cndmask_b32_e32 v219, v180, v219, vcc
	v_cndmask_b32_e32 v220, v180, v220, vcc
	v_cndmask_b32_e32 v221, v180, v221, vcc
	v_max3_f32 v155, v155, v218, v219
	v_max3_f32 v155, v155, v220, v221
	s_waitcnt lgkmcnt(4)
	v_mfma_f32_16x16x32_bf16 v[230:233], v[36:39], v[14:17], 0
	v_mfma_f32_16x16x32_bf16 v[230:233], v[40:43], v[10:13], v[230:233]
	ds_read_b128 v[60:63], v148 offset:30720
	ds_read_b128 v[64:67], v149 offset:30720
	s_add_i32 s17, s44, 32
	s_cmpk_lt_u32 s17, 0x800
	s_cselect_b64 vcc, -1, 0
	v_cndmask_b32_e32 v222, v180, v222, vcc
	v_cndmask_b32_e32 v223, v180, v223, vcc
	v_cndmask_b32_e32 v224, v180, v224, vcc
	v_cndmask_b32_e32 v225, v180, v225, vcc
	v_max3_f32 v155, v155, v222, v223
	v_max3_f32 v155, v155, v224, v225
	s_waitcnt lgkmcnt(4)
	v_mfma_f32_16x16x32_bf16 v[234:237], v[44:47], v[14:17], 0
	v_mfma_f32_16x16x32_bf16 v[234:237], v[48:51], v[10:13], v[234:237]
	ds_read_b128 v[36:39], v148 offset:32768
	ds_read_b128 v[40:43], v149 offset:32768
	s_add_i32 s17, s44, 48
	s_cmpk_lt_u32 s17, 0x800
	s_cselect_b64 vcc, -1, 0
	v_cndmask_b32_e32 v226, v180, v226, vcc
	v_cndmask_b32_e32 v227, v180, v227, vcc
	v_cndmask_b32_e32 v228, v180, v228, vcc
	v_cndmask_b32_e32 v229, v180, v229, vcc
	v_max3_f32 v155, v155, v226, v227
	v_max3_f32 v155, v155, v228, v229
	s_waitcnt lgkmcnt(4)
	v_mfma_f32_16x16x32_bf16 v[238:241], v[52:55], v[14:17], 0
	v_mfma_f32_16x16x32_bf16 v[238:241], v[56:59], v[10:13], v[238:241]
	s_add_i32 s17, s44, 64
	s_cmpk_lt_u32 s17, 0x800
	s_cselect_b64 vcc, -1, 0
	v_cndmask_b32_e32 v230, v180, v230, vcc
	v_cndmask_b32_e32 v231, v180, v231, vcc
	v_cndmask_b32_e32 v232, v180, v232, vcc
	v_cndmask_b32_e32 v233, v180, v233, vcc
	v_max3_f32 v155, v155, v230, v231
	v_max3_f32 v155, v155, v232, v233
	s_waitcnt lgkmcnt(2)
	v_mfma_f32_16x16x32_bf16 v[242:245], v[60:63], v[14:17], 0
	v_mfma_f32_16x16x32_bf16 v[242:245], v[64:67], v[10:13], v[242:245]
	s_add_i32 s17, s44, 80
	s_cmpk_lt_u32 s17, 0x800
	s_cselect_b64 vcc, -1, 0
	v_cndmask_b32_e32 v234, v180, v234, vcc
	v_cndmask_b32_e32 v235, v180, v235, vcc
	v_cndmask_b32_e32 v236, v180, v236, vcc
	v_cndmask_b32_e32 v237, v180, v237, vcc
	v_max3_f32 v155, v155, v234, v235
	v_max3_f32 v155, v155, v236, v237
	s_waitcnt lgkmcnt(0)
	v_mfma_f32_16x16x32_bf16 v[246:249], v[36:39], v[14:17], 0
	v_mfma_f32_16x16x32_bf16 v[246:249], v[40:43], v[10:13], v[246:249]
	s_add_i32 s17, s44, 96
	s_cmpk_lt_u32 s17, 0x800
	s_cselect_b64 vcc, -1, 0
	v_cndmask_b32_e32 v238, v180, v238, vcc
	v_cndmask_b32_e32 v239, v180, v239, vcc
	v_cndmask_b32_e32 v240, v180, v240, vcc
	v_cndmask_b32_e32 v241, v180, v241, vcc
	v_max3_f32 v155, v155, v238, v239
	v_max3_f32 v155, v155, v240, v241
	s_add_i32 s17, s44, 112
	s_cmpk_lt_u32 s17, 0x800
	s_cselect_b64 vcc, -1, 0
	v_cndmask_b32_e32 v242, v180, v242, vcc
	v_cndmask_b32_e32 v243, v180, v243, vcc
	v_cndmask_b32_e32 v244, v180, v244, vcc
	v_cndmask_b32_e32 v245, v180, v245, vcc
	v_max3_f32 v155, v155, v242, v243
	v_max3_f32 v155, v155, v244, v245
	s_add_i32 s17, s44, 128
	s_cmpk_lt_u32 s17, 0x800
	s_cselect_b64 s[0:1], -1, 0
	v_cmp_ge_i32_e32 vcc, 0, v150
	s_and_b64 vcc, vcc, s[0:1]
	v_cndmask_b32_e32 v246, v180, v246, vcc
	v_cmp_ge_i32_e32 vcc, -1, v150
	s_and_b64 vcc, vcc, s[0:1]
	v_cndmask_b32_e32 v247, v180, v247, vcc
	v_cmp_ge_i32_e32 vcc, -2, v150
	s_and_b64 vcc, vcc, s[0:1]
	v_cndmask_b32_e32 v248, v180, v248, vcc
	v_cmp_ge_i32_e32 vcc, -3, v150
	s_and_b64 vcc, vcc, s[0:1]
	v_cndmask_b32_e32 v249, v180, v249, vcc
	v_max3_f32 v155, v155, v246, v247
	v_max3_f32 v155, v155, v248, v249
	s_branch .Lattn_join_1
; #define LAS __attribute__((address_space(3)))
; __device__ __forceinline__ float kf(float x) { asm volatile("" : "+s"(x)); return x; }
; #define lds lds_hidden(lds0)
; __device__ __forceinline__ void attn_phase(LAS unsigned char* lds, const bf16_t* __restrict__ QA, const bf16_t* __restrict__ KA, const bf16_t* __restrict__ VTA, ...
;     ...
;             for (int i = 0; i < 18; ++i) {
;                 const LAS unsigned char* kp = lds + ((t0 + i) * 16 + l15) * KROW;
;                 const bf16x8 k0 = *(const LAS bf16x8*)(kp + kc0), k1 = *(const LAS bf16x8*)(kp + (kc0 ^ 64));
;                 f32x4 a = (f32x4){0.f, 0.f, 0.f, 0.f};
;                 a = __builtin_amdgcn_mfma_f32_16x16x32_bf16(k0, q0, a, 0, 0, 0);
;                 a = __builtin_amdgcn_mfma_f32_16x16x32_bf16(k1, q1, a, 0, 0, 0);
; #pragma unroll
;                 for (int r = 0; r < 4; ++r) {
;                     const int kap = (t0 + i) * 16 + 4 * g4 + r, rel = kap - qo, kpos = kb0 + kap;
;                     const bool ok = (rel >= 0) && (rel <= 256) && (kpos >= 0) && (kpos < SEQ);
;                     a[r] = ok ? a[r] : kf(-1e30f);
;                     mx = fmaxf(mx, a[r]);
;                 }
;                 sc[i] = a;
;             }
.Lattn_fast_1:
	s_waitcnt lgkmcnt(4)
	v_mfma_f32_16x16x32_bf16 v[182:185], v[36:39], v[14:17], 0
	v_mfma_f32_16x16x32_bf16 v[182:185], v[40:43], v[10:13], v[182:185]
	ds_read_b128 v[60:63], v148 offset:6144
	ds_read_b128 v[64:67], v149 offset:6144
	s_nop 1
	s_waitcnt lgkmcnt(4)
	v_mfma_f32_16x16x32_bf16 v[186:189], v[44:47], v[14:17], 0
	v_mfma_f32_16x16x32_bf16 v[186:189], v[48:51], v[10:13], v[186:189]
	ds_read_b128 v[36:39], v148 offset:8192
	ds_read_b128 v[40:43], v149 offset:8192
	s_nop 1
	s_waitcnt lgkmcnt(4)
	v_mfma_f32_16x16x32_bf16 v[190:193], v[52:55], v[14:17], 0
	v_mfma_f32_16x16x32_bf16 v[190:193], v[56:59], v[10:13], v[190:193]
	ds_read_b128 v[44:47], v148 offset:10240
	ds_read_b128 v[48:51], v149 offset:10240
	v_cmp_le_i32_e32 vcc, 0, v150
	v_cndmask_b32_e32 v182, v180, v182, vcc
	v_cmp_le_i32_e32 vcc, -1, v150
	v_cndmask_b32_e32 v183, v180, v183, vcc
	v_cmp_le_i32_e32 vcc, -2, v150
	v_cndmask_b32_e32 v184, v180, v184, vcc
	v_cmp_le_i32_e32 vcc, -3, v150
	v_cndmask_b32_e32 v185, v180, v185, vcc
	v_max3_f32 v155, v155, v182, v183
	v_max3_f32 v155, v155, v184, v185
	s_waitcnt lgkmcnt(4)
	v_mfma_f32_16x16x32_bf16 v[194:197], v[60:63], v[14:17], 0
	v_mfma_f32_16x16x32_bf16 v[194:197], v[64:67], v[10:13], v[194:197]
	ds_read_b128 v[52:55], v148 offset:12288
	ds_read_b128 v[56:59], v149 offset:12288
	v_max3_f32 v155, v155, v186, v187
	v_max3_f32 v155, v155, v188, v189
	s_waitcnt lgkmcnt(4)
	v_mfma_f32_16x16x32_bf16 v[198:201], v[36:39], v[14:17], 0
	v_mfma_f32_16x16x32_bf16 v[198:201], v[40:43], v[10:13], v[198:201]
	ds_read_b128 v[60:63], v148 offset:14336
	ds_read_b128 v[64:67], v149 offset:14336
	v_max3_f32 v155, v155, v190, v191
	v_max3_f32 v155, v155, v192, v193
	s_waitcnt lgkmcnt(4)
	v_mfma_f32_16x16x32_bf16 v[202:205], v[44:47], v[14:17], 0
	v_mfma_f32_16x16x32_bf16 v[202:205], v[48:51], v[10:13], v[202:205]
	ds_read_b128 v[36:39], v148 offset:16384
	ds_read_b128 v[40:43], v149 offset:16384
	v_max3_f32 v155, v155, v194, v195
	v_max3_f32 v155, v155, v196, v197
	s_waitcnt lgkmcnt(4)
	v_mfma_f32_16x16x32_bf16 v[206:209], v[52:55], v[14:17], 0
	v_mfma_f32_16x16x32_bf16 v[206:209], v[56:59], v[10:13], v[206:209]
	ds_read_b128 v[44:47], v148 offset:18432
	ds_read_b128 v[48:51], v149 offset:18432
	v_max3_f32 v155, v155, v198, v199
	v_max3_f32 v155, v155, v200, v201
	s_waitcnt lgkmcnt(4)
	v_mfma_f32_16x16x32_bf16 v[210:213], v[60:63], v[14:17], 0
	v_mfma_f32_16x16x32_bf16 v[210:213], v[64:67], v[10:13], v[210:213]
	ds_read_b128 v[52:55], v148 offset:20480
	ds_read_b128 v[56:59], v149 offset:20480
	v_max3_f32 v155, v155, v202, v203
	v_max3_f32 v155, v155, v204, v205
	s_waitcnt lgkmcnt(4)
	v_mfma_f32_16x16x32_bf16 v[214:217], v[36:39], v[14:17], 0
	v_mfma_f32_16x16x32_bf16 v[214:217], v[40:43], v[10:13], v[214:217]
	ds_read_b128 v[60:63], v148 offset:22528
	ds_read_b128 v[64:67], v149 offset:22528
	v_max3_f32 v155, v155, v206, v207
	v_max3_f32 v155, v155, v208, v209
	s_waitcnt lgkmcnt(4)
	v_mfma_f32_16x16x32_bf16 v[218:221], v[44:47], v[14:17], 0
	v_mfma_f32_16x16x32_bf16 v[218:221], v[48:51], v[10:13], v[218:221]
	ds_read_b128 v[36:39], v148 offset:24576
	ds_read_b128 v[40:43], v149 offset:24576
	v_max3_f32 v155, v155, v210, v211
	v_max3_f32 v155, v155, v212, v213
	s_waitcnt lgkmcnt(4)
	v_mfma_f32_16x16x32_bf16 v[222:225], v[52:55], v[14:17], 0
	v_mfma_f32_16x16x32_bf16 v[222:225], v[56:59], v[10:13], v[222:225]
	ds_read_b128 v[44:47], v148 offset:26624
	ds_read_b128 v[48:51], v149 offset:26624
	v_max3_f32 v155, v155, v214, v215
	v_max3_f32 v155, v155, v216, v217
	s_waitcnt lgkmcnt(4)
	v_mfma_f32_16x16x32_bf16 v[226:229], v[60:63], v[14:17], 0
	v_mfma_f32_16x16x32_bf16 v[226:229], v[64:67], v[10:13], v[226:229]
	ds_read_b128 v[52:55], v148 offset:28672
	ds_read_b128 v[56:59], v149 offset:28672
	v_max3_f32 v155, v155, v218, v219
	v_max3_f32 v155, v155, v220, v221
	s_waitcnt lgkmcnt(4)
	v_mfma_f32_16x16x32_bf16 v[230:233], v[36:39], v[14:17], 0
	v_mfma_f32_16x16x32_bf16 v[230:233], v[40:43], v[10:13], v[230:233]
	ds_read_b128 v[60:63], v148 offset:30720
	ds_read_b128 v[64:67], v149 offset:30720
	v_max3_f32 v155, v155, v222, v223
	v_max3_f32 v155, v155, v224, v225
	s_waitcnt lgkmcnt(4)
	v_mfma_f32_16x16x32_bf16 v[234:237], v[44:47], v[14:17], 0
	v_mfma_f32_16x16x32_bf16 v[234:237], v[48:51], v[10:13], v[234:237]
	ds_read_b128 v[36:39], v148 offset:32768
	ds_read_b128 v[40:43], v149 offset:32768
	v_max3_f32 v155, v155, v226, v227
	v_max3_f32 v155, v155, v228, v229
	s_waitcnt lgkmcnt(4)
	v_mfma_f32_16x16x32_bf16 v[238:241], v[52:55], v[14:17], 0
	v_mfma_f32_16x16x32_bf16 v[238:241], v[56:59], v[10:13], v[238:241]
	v_max3_f32 v155, v155, v230, v231
	v_max3_f32 v155, v155, v232, v233
	s_waitcnt lgkmcnt(2)
	v_mfma_f32_16x16x32_bf16 v[242:245], v[60:63], v[14:17], 0
	v_mfma_f32_16x16x32_bf16 v[242:245], v[64:67], v[10:13], v[242:245]
	v_max3_f32 v155, v155, v234, v235
	v_max3_f32 v155, v155, v236, v237
	s_waitcnt lgkmcnt(0)
	v_mfma_f32_16x16x32_bf16 v[246:249], v[36:39], v[14:17], 0
	v_mfma_f32_16x16x32_bf16 v[246:249], v[40:43], v[10:13], v[246:249]
	v_max3_f32 v155, v155, v238, v239
	v_max3_f32 v155, v155, v240, v241
	s_nop 3
	v_max3_f32 v155, v155, v242, v243
	v_max3_f32 v155, v155, v244, v245
	v_cmp_ge_i32_e32 vcc, 0, v150
	v_cndmask_b32_e32 v246, v180, v246, vcc
	v_cmp_ge_i32_e32 vcc, -1, v150
	v_cndmask_b32_e32 v247, v180, v247, vcc
	v_cmp_ge_i32_e32 vcc, -2, v150
	v_cndmask_b32_e32 v248, v180, v248, vcc
	v_cmp_ge_i32_e32 vcc, -3, v150
	v_cndmask_b32_e32 v249, v180, v249, vcc
	v_max3_f32 v155, v155, v246, v247
	v_max3_f32 v155, v155, v248, v249
; __device__ __forceinline__ float fexp(float x) { return __builtin_amdgcn_exp2f(x * 1.4426950408889634f); }
; __device__ __forceinline__ float shx(float v, int m) { int ln; asm volatile("v_mbcnt_lo_u32_b32 %0, -1, 0\n\tv_mbcnt_hi_u32_b32 %0, -1, %0" : "=v"(ln)); return __builtin_bit_cast(float, __builtin_amdgcn_ds_bpermute((ln ^ m) << 2, __builtin_bit_cast(int, v))); }
; __device__ __forceinline__ void attn_phase(LAS unsigned char* lds, const bf16_t* __restrict__ QA, const bf16_t* __restrict__ KA, const bf16_t* __restrict__ VTA, ...
;     ...
;             mx = fmaxf(mx, shx(mx, 16)); mx = fmaxf(mx, shx(mx, 32));
;             float sum = 0.f;
; #pragma unroll
;             for (int i = 0; i < 18; ++i)
; #pragma unroll
;                 for (int r = 0; r < 4; ++r) { const float p = fexp(sc[i][r] - mx); sc[i][r] = p; sum += p; }
;             sum += shx(sum, 16); sum += shx(sum, 32);
;             sum += fexp(sk - mx);
.Lattn_join_1:
	ds_bpermute_b32 v160, v158, v155
	s_waitcnt lgkmcnt(0)
	v_max_f32_e32 v155, v155, v160
	ds_bpermute_b32 v160, v159, v155
	ds_read2_b64 v[76:79], v151 offset0:0 offset1:4
	ds_read2_b64 v[80:83], v152 offset0:0 offset1:4
	ds_read2_b64 v[84:87], v153 offset0:0 offset1:4
	ds_read2_b64 v[162:165], v154 offset0:0 offset1:4
	ds_read2_b64 v[166:169], v151 offset0:8 offset1:12
	s_waitcnt lgkmcnt(5)
	v_max_f32_e32 v155, v155, v160
	v_mul_f32_e64 v174, -v155, s16
	v_mov_b32_e32 v157, v174
	v_pk_fma_f32 v[182:183], v[182:183], s[16:17], v[174:175] op_sel_hi:[1,0,0]
	v_pk_fma_f32 v[184:185], v[184:185], s[16:17], v[174:175] op_sel_hi:[1,0,0]
	v_pk_fma_f32 v[186:187], v[186:187], s[16:17], v[174:175] op_sel_hi:[1,0,0]
	v_pk_fma_f32 v[188:189], v[188:189], s[16:17], v[174:175] op_sel_hi:[1,0,0]
	v_pk_fma_f32 v[190:191], v[190:191], s[16:17], v[174:175] op_sel_hi:[1,0,0]
	v_pk_fma_f32 v[192:193], v[192:193], s[16:17], v[174:175] op_sel_hi:[1,0,0]
	v_pk_fma_f32 v[194:195], v[194:195], s[16:17], v[174:175] op_sel_hi:[1,0,0]
	v_pk_fma_f32 v[196:197], v[196:197], s[16:17], v[174:175] op_sel_hi:[1,0,0]
	v_pk_fma_f32 v[198:199], v[198:199], s[16:17], v[174:175] op_sel_hi:[1,0,0]
	v_pk_fma_f32 v[200:201], v[200:201], s[16:17], v[174:175] op_sel_hi:[1,0,0]
	v_pk_fma_f32 v[202:203], v[202:203], s[16:17], v[174:175] op_sel_hi:[1,0,0]
	v_pk_fma_f32 v[204:205], v[204:205], s[16:17], v[174:175] op_sel_hi:[1,0,0]
	v_pk_fma_f32 v[206:207], v[206:207], s[16:17], v[174:175] op_sel_hi:[1,0,0]
	v_pk_fma_f32 v[208:209], v[208:209], s[16:17], v[174:175] op_sel_hi:[1,0,0]
	v_pk_fma_f32 v[210:211], v[210:211], s[16:17], v[174:175] op_sel_hi:[1,0,0]
	v_pk_fma_f32 v[212:213], v[212:213], s[16:17], v[174:175] op_sel_hi:[1,0,0]
	v_pk_fma_f32 v[214:215], v[214:215], s[16:17], v[174:175] op_sel_hi:[1,0,0]
	v_pk_fma_f32 v[216:217], v[216:217], s[16:17], v[174:175] op_sel_hi:[1,0,0]
	v_pk_fma_f32 v[218:219], v[218:219], s[16:17], v[174:175] op_sel_hi:[1,0,0]
	v_pk_fma_f32 v[220:221], v[220:221], s[16:17], v[174:175] op_sel_hi:[1,0,0]
	v_pk_fma_f32 v[222:223], v[222:223], s[16:17], v[174:175] op_sel_hi:[1,0,0]
	v_pk_fma_f32 v[224:225], v[224:225], s[16:17], v[174:175] op_sel_hi:[1,0,0]
	v_pk_fma_f32 v[226:227], v[226:227], s[16:17], v[174:175] op_sel_hi:[1,0,0]
	v_pk_fma_f32 v[228:229], v[228:229], s[16:17], v[174:175] op_sel_hi:[1,0,0]
	v_pk_fma_f32 v[230:231], v[230:231], s[16:17], v[174:175] op_sel_hi:[1,0,0]
	v_pk_fma_f32 v[232:233], v[232:233], s[16:17], v[174:175] op_sel_hi:[1,0,0]
	v_pk_fma_f32 v[234:235], v[234:235], s[16:17], v[174:175] op_sel_hi:[1,0,0]
	v_pk_fma_f32 v[236:237], v[236:237], s[16:17], v[174:175] op_sel_hi:[1,0,0]
	v_pk_fma_f32 v[238:239], v[238:239], s[16:17], v[174:175] op_sel_hi:[1,0,0]
	v_pk_fma_f32 v[240:241], v[240:241], s[16:17], v[174:175] op_sel_hi:[1,0,0]
	v_pk_fma_f32 v[242:243], v[242:243], s[16:17], v[174:175] op_sel_hi:[1,0,0]
	v_pk_fma_f32 v[244:245], v[244:245], s[16:17], v[174:175] op_sel_hi:[1,0,0]
	v_pk_fma_f32 v[246:247], v[246:247], s[16:17], v[174:175] op_sel_hi:[1,0,0]
	v_pk_fma_f32 v[248:249], v[248:249], s[16:17], v[174:175] op_sel_hi:[1,0,0]
	v_exp_f32_e32 v182, v182
	v_exp_f32_e32 v183, v183
	v_exp_f32_e32 v184, v184
	v_exp_f32_e32 v185, v185
	v_mov_b32_e32 v176, v182
	v_mov_b32_e32 v177, v183
	v_exp_f32_e32 v186, v186
	v_exp_f32_e32 v187, v187
	v_pk_add_f32 v[176:177], v[176:177], v[184:185]
	v_exp_f32_e32 v188, v188
	v_exp_f32_e32 v189, v189
	v_pk_add_f32 v[176:177], v[176:177], v[186:187]
	v_exp_f32_e32 v190, v190
	v_exp_f32_e32 v191, v191
	v_pk_add_f32 v[176:177], v[176:177], v[188:189]
	v_exp_f32_e32 v192, v192
	v_exp_f32_e32 v193, v193
	v_pk_add_f32 v[176:177], v[176:177], v[190:191]
	v_exp_f32_e32 v194, v194
	v_exp_f32_e32 v195, v195
	v_pk_add_f32 v[176:177], v[176:177], v[192:193]
	v_exp_f32_e32 v196, v196
	v_exp_f32_e32 v197, v197
	v_pk_add_f32 v[176:177], v[176:177], v[194:195]
	v_exp_f32_e32 v198, v198
	v_exp_f32_e32 v199, v199
	v_pk_add_f32 v[176:177], v[176:177], v[196:197]
	v_exp_f32_e32 v200, v200
	v_exp_f32_e32 v201, v201
	v_pk_add_f32 v[176:177], v[176:177], v[198:199]
	v_exp_f32_e32 v202, v202
	v_exp_f32_e32 v203, v203
	v_pk_add_f32 v[176:177], v[176:177], v[200:201]
	v_exp_f32_e32 v204, v204
	v_exp_f32_e32 v205, v205
	v_pk_add_f32 v[176:177], v[176:177], v[202:203]
	v_exp_f32_e32 v206, v206
	v_exp_f32_e32 v207, v207
	v_pk_add_f32 v[176:177], v[176:177], v[204:205]
	v_exp_f32_e32 v208, v208
	v_exp_f32_e32 v209, v209
	v_pk_add_f32 v[176:177], v[176:177], v[206:207]
	v_exp_f32_e32 v210, v210
	v_exp_f32_e32 v211, v211
	v_pk_add_f32 v[176:177], v[176:177], v[208:209]
	v_exp_f32_e32 v212, v212
	v_exp_f32_e32 v213, v213
	v_pk_add_f32 v[176:177], v[176:177], v[210:211]
	v_exp_f32_e32 v214, v214
	v_exp_f32_e32 v215, v215
	v_pk_add_f32 v[176:177], v[176:177], v[212:213]
	v_exp_f32_e32 v216, v216
	v_exp_f32_e32 v217, v217
	v_pk_add_f32 v[176:177], v[176:177], v[214:215]
	v_exp_f32_e32 v218, v218
	v_exp_f32_e32 v219, v219
	v_pk_add_f32 v[176:177], v[176:177], v[216:217]
	v_exp_f32_e32 v220, v220
	v_exp_f32_e32 v221, v221
	v_pk_add_f32 v[176:177], v[176:177], v[218:219]
	v_exp_f32_e32 v222, v222
	v_exp_f32_e32 v223, v223
	v_pk_add_f32 v[176:177], v[176:177], v[220:221]
	v_exp_f32_e32 v224, v224
	v_exp_f32_e32 v225, v225
	v_pk_add_f32 v[176:177], v[176:177], v[222:223]
	v_exp_f32_e32 v226, v226
	v_exp_f32_e32 v227, v227
	v_pk_add_f32 v[176:177], v[176:177], v[224:225]
	v_exp_f32_e32 v228, v228
	v_exp_f32_e32 v229, v229
	v_pk_add_f32 v[176:177], v[176:177], v[226:227]
	v_exp_f32_e32 v230, v230
	v_exp_f32_e32 v231, v231
	v_pk_add_f32 v[176:177], v[176:177], v[228:229]
	v_exp_f32_e32 v232, v232
	v_exp_f32_e32 v233, v233
	v_pk_add_f32 v[176:177], v[176:177], v[230:231]
	v_exp_f32_e32 v234, v234
	v_exp_f32_e32 v235, v235
	v_pk_add_f32 v[176:177], v[176:177], v[232:233]
	v_exp_f32_e32 v236, v236
	v_exp_f32_e32 v237, v237
	v_pk_add_f32 v[176:177], v[176:177], v[234:235]
	v_exp_f32_e32 v238, v238
	v_exp_f32_e32 v239, v239
	v_pk_add_f32 v[176:177], v[176:177], v[236:237]
	v_exp_f32_e32 v240, v240
	v_exp_f32_e32 v241, v241
	v_pk_add_f32 v[176:177], v[176:177], v[238:239]
	v_exp_f32_e32 v242, v242
	v_exp_f32_e32 v243, v243
	v_pk_add_f32 v[176:177], v[176:177], v[240:241]
	v_exp_f32_e32 v244, v244
	v_exp_f32_e32 v245, v245
	v_pk_add_f32 v[176:177], v[176:177], v[242:243]
	v_exp_f32_e32 v246, v246
	v_exp_f32_e32 v247, v247
	v_pk_add_f32 v[176:177], v[176:177], v[244:245]
	v_exp_f32_e32 v248, v248
	v_exp_f32_e32 v249, v249
	v_pk_add_f32 v[176:177], v[176:177], v[246:247]
	s_nop 0
	v_pk_add_f32 v[176:177], v[176:177], v[248:249]
	v_add_f32_e32 v156, v176, v177
	v_fma_f32 v161, v144, s16, v157
	v_exp_f32_e32 v161, v161
	ds_bpermute_b32 v160, v158, v156
	v_cvt_pk_bf16_f32 v68, v182, v183
	v_cvt_pk_bf16_f32 v69, v184, v185
	v_cvt_pk_bf16_f32 v70, v186, v187
	v_cvt_pk_bf16_f32 v71, v188, v189
	s_waitcnt lgkmcnt(0)
; #define LAS __attribute__((address_space(3)))
; __device__ __forceinline__ unsigned cvt_pk_bf16(float lo, float hi) { const bf16x2_t r = __builtin_convertvector((f32x2_t){lo, hi}, bf16x2_t); return __builtin_bit_cast(unsigned, r); }
; __device__ __forceinline__ float fexp(float x) { return __builtin_amdgcn_exp2f(x * 1.4426950408889634f); }
; __device__ __forceinline__ float shx(float v, int m) { int ln; asm volatile("v_mbcnt_lo_u32_b32 %0, -1, 0\n\tv_mbcnt_hi_u32_b32 %0, -1, %0" : "=v"(ln)); return __builtin_bit_cast(float, __builtin_amdgcn_ds_bpermute((ln ^ m) << 2, __builtin_bit_cast(int, v))); }
; #define lds lds_hidden(lds0)
; __device__ __forceinline__ void attn_phase(LAS unsigned char* lds, const bf16_t* __restrict__ QA, const bf16_t* __restrict__ KA, const bf16_t* __restrict__ VTA, ...
;     ...
;                 for (int r = 0; r < 4; ++r) { const float p = fexp(sc[i][r] - mx); sc[i][r] = p; sum += p; }
;             sum += shx(sum, 16); sum += shx(sum, 32);
;             sum += fexp(sk - mx);
;             f32x4 o[4];
; #pragma unroll
;             for (int dt = 0; dt < 4; ++dt) o[dt] = (f32x4){0.f, 0.f, 0.f, 0.f};
; #pragma unroll
;             for (int u = 0; u < 9; ++u) {
;                 u32x4 pw; pw.x = cvt_pk_bf16(sc[2 * u][0], sc[2 * u][1]); pw.y = cvt_pk_bf16(sc[2 * u][2], sc[2 * u][3]);
;                 pw.z = cvt_pk_bf16(sc[2 * u + 1][0], sc[2 * u + 1][1]); pw.w = cvt_pk_bf16(sc[2 * u + 1][2], sc[2 * u + 1][3]);
;                 const bf16x8 pf = __builtin_bit_cast(bf16x8, pw);
; #pragma unroll
;                 for (int dt = 0; dt < 4; ++dt) {
;                     const LAS unsigned char* vp = lds + V_OFF + (dt * 16 + l15) * VROW + ((t0 + 2 * u) * 16 + 4 * g4) * 2;
;                     const u32x2 va = *(const LAS u32x2*)vp, vb = *(const LAS u32x2*)(vp + 32);
;                     const bf16x8 vf = __builtin_bit_cast(bf16x8, (u32x4){va.x, va.y, vb.x, vb.y});
;                     o[dt] = __builtin_amdgcn_mfma_f32_16x16x32_bf16(vf, pf, o[dt], 0, 0, 0);
;                 }
;             }
	v_add_f32_e32 v156, v156, v160
	ds_bpermute_b32 v160, v159, v156
	v_cvt_pk_bf16_f32 v72, v190, v191
	v_cvt_pk_bf16_f32 v73, v192, v193
	v_cvt_pk_bf16_f32 v74, v194, v195
	v_cvt_pk_bf16_f32 v75, v196, v197
	v_mfma_f32_16x16x32_bf16 v[18:21], v[76:79], v[68:71], 0
	ds_read2_b64 v[170:173], v152 offset0:8 offset1:12
	v_mfma_f32_16x16x32_bf16 v[22:25], v[80:83], v[68:71], 0
	ds_read2_b64 v[76:79], v153 offset0:8 offset1:12
	v_mfma_f32_16x16x32_bf16 v[26:29], v[84:87], v[68:71], 0
	ds_read2_b64 v[80:83], v154 offset0:8 offset1:12
	v_mfma_f32_16x16x32_bf16 v[30:33], v[162:165], v[68:71], 0
	ds_read2_b64 v[84:87], v151 offset0:16 offset1:20
	v_cvt_pk_bf16_f32 v68, v198, v199
	v_cvt_pk_bf16_f32 v69, v200, v201
	v_cvt_pk_bf16_f32 v70, v202, v203
	v_cvt_pk_bf16_f32 v71, v204, v205
	v_mfma_f32_16x16x32_bf16 v[18:21], v[166:169], v[72:75], v[18:21]
	ds_read2_b64 v[162:165], v152 offset0:16 offset1:20
	s_waitcnt lgkmcnt(4)
	v_add_f32_e32 v156, v156, v160
	v_add_f32_e32 v156, v156, v161
	v_mfma_f32_16x16x32_bf16 v[22:25], v[170:173], v[72:75], v[22:25]
	ds_read2_b64 v[166:169], v153 offset0:16 offset1:20
	s_waitcnt lgkmcnt(4)
	v_mfma_f32_16x16x32_bf16 v[26:29], v[76:79], v[72:75], v[26:29]
	ds_read2_b64 v[170:173], v154 offset0:16 offset1:20
	s_waitcnt lgkmcnt(4)
	v_mfma_f32_16x16x32_bf16 v[30:33], v[80:83], v[72:75], v[30:33]
	ds_read2_b64 v[76:79], v151 offset0:24 offset1:28
	v_cvt_pk_bf16_f32 v72, v206, v207
	v_cvt_pk_bf16_f32 v73, v208, v209
	v_cvt_pk_bf16_f32 v74, v210, v211
	v_cvt_pk_bf16_f32 v75, v212, v213
	s_waitcnt lgkmcnt(4)
	v_mfma_f32_16x16x32_bf16 v[18:21], v[84:87], v[68:71], v[18:21]
	ds_read2_b64 v[80:83], v152 offset0:24 offset1:28
	s_waitcnt lgkmcnt(4)
	v_mfma_f32_16x16x32_bf16 v[22:25], v[162:165], v[68:71], v[22:25]
	ds_read2_b64 v[84:87], v153 offset0:24 offset1:28
	s_waitcnt lgkmcnt(4)
	v_mfma_f32_16x16x32_bf16 v[26:29], v[166:169], v[68:71], v[26:29]
	ds_read2_b64 v[162:165], v154 offset0:24 offset1:28
	s_waitcnt lgkmcnt(4)
	v_mfma_f32_16x16x32_bf16 v[30:33], v[170:173], v[68:71], v[30:33]
	ds_read2_b64 v[166:169], v151 offset0:32 offset1:36
	v_cvt_pk_bf16_f32 v68, v214, v215
	v_cvt_pk_bf16_f32 v69, v216, v217
	v_cvt_pk_bf16_f32 v70, v218, v219
	v_cvt_pk_bf16_f32 v71, v220, v221
	s_waitcnt lgkmcnt(4)
	v_mfma_f32_16x16x32_bf16 v[18:21], v[76:79], v[72:75], v[18:21]
	ds_read2_b64 v[170:173], v152 offset0:32 offset1:36
	s_waitcnt lgkmcnt(4)
	v_mfma_f32_16x16x32_bf16 v[22:25], v[80:83], v[72:75], v[22:25]
	ds_read2_b64 v[76:79], v153 offset0:32 offset1:36
	s_waitcnt lgkmcnt(4)
	v_mfma_f32_16x16x32_bf16 v[26:29], v[84:87], v[72:75], v[26:29]
	ds_read2_b64 v[80:83], v154 offset0:32 offset1:36
	s_waitcnt lgkmcnt(4)
	v_mfma_f32_16x16x32_bf16 v[30:33], v[162:165], v[72:75], v[30:33]
	ds_read2_b64 v[84:87], v151 offset0:40 offset1:44
	v_cvt_pk_bf16_f32 v72, v222, v223
	v_cvt_pk_bf16_f32 v73, v224, v225
	v_cvt_pk_bf16_f32 v74, v226, v227
	v_cvt_pk_bf16_f32 v75, v228, v229
	s_waitcnt lgkmcnt(4)
	v_mfma_f32_16x16x32_bf16 v[18:21], v[166:169], v[68:71], v[18:21]
	ds_read2_b64 v[162:165], v152 offset0:40 offset1:44
	s_waitcnt lgkmcnt(4)
	v_mfma_f32_16x16x32_bf16 v[22:25], v[170:173], v[68:71], v[22:25]
	ds_read2_b64 v[166:169], v153 offset0:40 offset1:44
	s_waitcnt lgkmcnt(4)
	v_mfma_f32_16x16x32_bf16 v[26:29], v[76:79], v[68:71], v[26:29]
	ds_read2_b64 v[170:173], v154 offset0:40 offset1:44
	s_waitcnt lgkmcnt(4)
	v_mfma_f32_16x16x32_bf16 v[30:33], v[80:83], v[68:71], v[30:33]
	ds_read2_b64 v[76:79], v151 offset0:48 offset1:52
	v_cvt_pk_bf16_f32 v68, v230, v231
	v_cvt_pk_bf16_f32 v69, v232, v233
	v_cvt_pk_bf16_f32 v70, v234, v235
	v_cvt_pk_bf16_f32 v71, v236, v237
	s_waitcnt lgkmcnt(4)
	v_mfma_f32_16x16x32_bf16 v[18:21], v[84:87], v[72:75], v[18:21]
	ds_read2_b64 v[80:83], v152 offset0:48 offset1:52
	s_waitcnt lgkmcnt(4)
	v_mfma_f32_16x16x32_bf16 v[22:25], v[162:165], v[72:75], v[22:25]
	ds_read2_b64 v[84:87], v153 offset0:48 offset1:52
	s_waitcnt lgkmcnt(4)
	v_mfma_f32_16x16x32_bf16 v[26:29], v[166:169], v[72:75], v[26:29]
	ds_read2_b64 v[162:165], v154 offset0:48 offset1:52
	s_waitcnt lgkmcnt(4)
; #define LAS __attribute__((address_space(3)))
; __device__ __forceinline__ unsigned cvt_pk_bf16(float lo, float hi) { const bf16x2_t r = __builtin_convertvector((f32x2_t){lo, hi}, bf16x2_t); return __builtin_bit_cast(unsigned, r); }
; __device__ __forceinline__ float shx(float v, int m) { int ln; asm volatile("v_mbcnt_lo_u32_b32 %0, -1, 0\n\tv_mbcnt_hi_u32_b32 %0, -1, %0" : "=v"(ln)); return __builtin_bit_cast(float, __builtin_amdgcn_ds_bpermute((ln ^ m) << 2, __builtin_bit_cast(int, v))); }
; #define lds lds_hidden(lds0)
; #define SSQ WSP(float, W_SSQ)
; __device__ __forceinline__ void attn_phase(LAS unsigned char* lds, const bf16_t* __restrict__ QA, const bf16_t* __restrict__ KA, const bf16_t* __restrict__ VTA, ...
;     ...
;             for (int u = 0; u < 9; ++u) {
;                 u32x4 pw; pw.x = cvt_pk_bf16(sc[2 * u][0], sc[2 * u][1]); pw.y = cvt_pk_bf16(sc[2 * u][2], sc[2 * u][3]);
;                 pw.z = cvt_pk_bf16(sc[2 * u + 1][0], sc[2 * u + 1][1]); pw.w = cvt_pk_bf16(sc[2 * u + 1][2], sc[2 * u + 1][3]);
;                 const bf16x8 pf = __builtin_bit_cast(bf16x8, pw);
; #pragma unroll
;                 for (int dt = 0; dt < 4; ++dt) {
;                     const LAS unsigned char* vp = lds + V_OFF + (dt * 16 + l15) * VROW + ((t0 + 2 * u) * 16 + 4 * g4) * 2;
;                     const u32x2 va = *(const LAS u32x2*)vp, vb = *(const LAS u32x2*)(vp + 32);
;                     const bf16x8 vf = __builtin_bit_cast(bf16x8, (u32x4){va.x, va.y, vb.x, vb.y});
;                     o[dt] = __builtin_amdgcn_mfma_f32_16x16x32_bf16(vf, pf, o[dt], 0, 0, 0);
;                 }
;             }
;             const float inv = 1.f / sum;
;             float ss = 0.f;
; #pragma unroll
;             for (int dt = 0; dt < 4; ++dt) {
;                 const f32x4 v = o[dt] * inv;
;                 ss += v[0] * v[0] + v[1] * v[1] + v[2] * v[2] + v[3] * v[3];
;                 u32x2 w; w.x = cvt_pk_bf16(v[0], v[1]); w.y = cvt_pk_bf16(v[2], v[3]);
;                 *(u32x2*)(AO + tok * 512 + head * 64 + dt * 16 + 4 * g4) = w;
;             }
;             ss += shx(ss, 16); ss += shx(ss, 32);
;             if (g4 == 0) SSQ[tok * 8 + head] = ss;
	v_mfma_f32_16x16x32_bf16 v[30:33], v[170:173], v[72:75], v[30:33]
	ds_read2_b64 v[166:169], v151 offset0:56 offset1:60
	v_cvt_pk_bf16_f32 v72, v238, v239
	v_cvt_pk_bf16_f32 v73, v240, v241
	v_cvt_pk_bf16_f32 v74, v242, v243
	v_cvt_pk_bf16_f32 v75, v244, v245
	s_waitcnt lgkmcnt(4)
	v_mfma_f32_16x16x32_bf16 v[18:21], v[76:79], v[68:71], v[18:21]
	ds_read2_b64 v[170:173], v152 offset0:56 offset1:60
	s_waitcnt lgkmcnt(4)
	v_mfma_f32_16x16x32_bf16 v[22:25], v[80:83], v[68:71], v[22:25]
	ds_read2_b64 v[76:79], v153 offset0:56 offset1:60
	s_waitcnt lgkmcnt(4)
	v_mfma_f32_16x16x32_bf16 v[26:29], v[84:87], v[68:71], v[26:29]
	ds_read2_b64 v[80:83], v154 offset0:56 offset1:60
	s_waitcnt lgkmcnt(4)
	v_mfma_f32_16x16x32_bf16 v[30:33], v[162:165], v[68:71], v[30:33]
	ds_read2_b64 v[84:87], v151 offset0:64 offset1:68
	v_cvt_pk_bf16_f32 v68, v246, v247
	v_cvt_pk_bf16_f32 v69, v248, v249
	v_mov_b32_e32 v70, 0
	v_mov_b32_e32 v71, 0
	s_waitcnt lgkmcnt(4)
	v_mfma_f32_16x16x32_bf16 v[18:21], v[166:169], v[72:75], v[18:21]
	ds_read2_b64 v[162:165], v152 offset0:64 offset1:68
	s_waitcnt lgkmcnt(4)
	v_mfma_f32_16x16x32_bf16 v[22:25], v[170:173], v[72:75], v[22:25]
	ds_read2_b64 v[166:169], v153 offset0:64 offset1:68
	s_waitcnt lgkmcnt(4)
	v_mfma_f32_16x16x32_bf16 v[26:29], v[76:79], v[72:75], v[26:29]
	ds_read2_b64 v[170:173], v154 offset0:64 offset1:68
	s_waitcnt lgkmcnt(4)
	v_mfma_f32_16x16x32_bf16 v[30:33], v[80:83], v[72:75], v[30:33]
	s_waitcnt lgkmcnt(3)
	v_mfma_f32_16x16x32_bf16 v[18:21], v[84:87], v[68:71], v[18:21]
	s_waitcnt lgkmcnt(2)
	v_mfma_f32_16x16x32_bf16 v[22:25], v[162:165], v[68:71], v[22:25]
	s_waitcnt lgkmcnt(1)
	v_mfma_f32_16x16x32_bf16 v[26:29], v[166:169], v[68:71], v[26:29]
	s_waitcnt lgkmcnt(0)
	v_mfma_f32_16x16x32_bf16 v[30:33], v[170:173], v[68:71], v[30:33]
	v_div_scale_f32 v174, s[0:1], v156, v156, 1.0
	v_rcp_f32_e32 v175, v174
	s_nop 0
	v_fma_f32 v176, -v174, v175, 1.0
	v_fmac_f32_e32 v175, v176, v175
	v_div_scale_f32 v176, vcc, 1.0, v156, 1.0
	v_mul_f32_e32 v177, v176, v175
	v_fma_f32 v178, -v174, v177, v176
	v_fmac_f32_e32 v177, v178, v175
	v_fma_f32 v174, -v174, v177, v176
	v_div_fmas_f32 v174, v174, v175, v177
	v_div_fixup_f32 v179, v174, v156, 1.0
	v_lshl_add_u64 v[176:177], v[112:113], 0, s[26:27]
	v_mul_f32_e32 v18, v179, v18
	v_mul_f32_e32 v19, v179, v19
	v_mul_f32_e32 v20, v179, v20
	v_mul_f32_e32 v21, v179, v21
	v_mul_f32_e32 v178, v18, v18
	v_fmac_f32_e32 v178, v19, v19
	v_fmac_f32_e32 v178, v20, v20
	v_fmac_f32_e32 v178, v21, v21
	v_cvt_pk_bf16_f32 v36, v18, v19
	v_cvt_pk_bf16_f32 v37, v20, v21
	global_store_dwordx2 v[176:177], v[36:37], off
	v_mul_f32_e32 v22, v179, v22
	v_mul_f32_e32 v23, v179, v23
	v_mul_f32_e32 v24, v179, v24
	v_mul_f32_e32 v25, v179, v25
	v_fmac_f32_e32 v178, v22, v22
	v_fmac_f32_e32 v178, v23, v23
	v_fmac_f32_e32 v178, v24, v24
	v_fmac_f32_e32 v178, v25, v25
	v_cvt_pk_bf16_f32 v38, v22, v23
	v_cvt_pk_bf16_f32 v39, v24, v25
	global_store_dwordx2 v[176:177], v[38:39], off offset:32
	v_mul_f32_e32 v26, v179, v26
	v_mul_f32_e32 v27, v179, v27
	v_mul_f32_e32 v28, v179, v28
	v_mul_f32_e32 v29, v179, v29
	v_fmac_f32_e32 v178, v26, v26
	v_fmac_f32_e32 v178, v27, v27
	v_fmac_f32_e32 v178, v28, v28
	v_fmac_f32_e32 v178, v29, v29
	v_cvt_pk_bf16_f32 v40, v26, v27
	v_cvt_pk_bf16_f32 v41, v28, v29
	global_store_dwordx2 v[176:177], v[40:41], off offset:64
	v_mul_f32_e32 v30, v179, v30
	v_mul_f32_e32 v31, v179, v31
	v_mul_f32_e32 v32, v179, v32
	v_mul_f32_e32 v33, v179, v33
	v_fmac_f32_e32 v178, v30, v30
	v_fmac_f32_e32 v178, v31, v31
	v_fmac_f32_e32 v178, v32, v32
	v_fmac_f32_e32 v178, v33, v33
	v_cvt_pk_bf16_f32 v42, v30, v31
	v_cvt_pk_bf16_f32 v43, v32, v33
	global_store_dwordx2 v[176:177], v[42:43], off offset:96
	ds_bpermute_b32 v160, v158, v178
	s_waitcnt lgkmcnt(0)
	v_add_f32_e32 v10, v178, v160
	ds_bpermute_b32 v11, v159, v10
	s_and_saveexec_b64 s[0:1], s[8:9]
	s_cbranch_execz .LBB0_773
	s_waitcnt lgkmcnt(0)
	v_add_f32_e32 v10, v10, v11
	global_store_dword v[108:109], v10, off
	s_branch .LBB0_773

; #define LAS __attribute__((address_space(3)))
; __device__ __forceinline__ bf16_t f2bf(float f) { unsigned u = __float_as_uint(f); u += 0x7FFFu + ((u >> 16) & 1u); return (bf16_t)(u >> 16); }
; __device__ __forceinline__ float fexp(float x) { return __builtin_amdgcn_exp2f(x * 1.4426950408889634f); }
; #define lds lds_hidden(lds0)
; __device__ __forceinline__ void c3_phase(LAS unsigned char* lds, const bf16_t* __restrict__ QH, const bf16_t* __restrict__ LF, const bf16_t* __restrict__ VTH, const bf16_t* __restrict__ SIN, ...
;     ...
;             for (int i = 0; i < 16; ++i) lfv[i] = __uint_as_float(lfn[i] << 16);
; #pragma unroll
;             for (int i = 0; i < 4; ++i) stv[i] = stn[i];
;             float run = 0.f;
; #pragma unroll
;             for (int i = 0; i < 16; ++i) { run += lfv[i]; cs[i] = run; }
;             __syncthreads();
;             qtot[tq * 128 + d] = run;
; #pragma unroll
;             for (int i = 0; i < 4; ++i) { const int ch = tid + i * 512, e = ch >> 4, part = ch & 15;
;                 *(LAS u32x4*)(lds + C3_ST + e * R272 + part * 16) = stv[i]; }
;             __syncthreads();
;             const float q0 = qtot[d], q1 = qtot[128 + d], q2 = qtot[256 + d], q3 = qtot[384 + d];
;             const float pre = (tq > 0 ? q0 : 0.f) + (tq > 1 ? q1 : 0.f) + (tq > 2 ? q2 : 0.f), total = (q0 + q1) + (q2 + q3);
;             const float mref = dir == 0 ? (q0 + q1) : (q2 + q3);
; #pragma unroll
;             for (int i = 0; i < 16; ++i) {
;                 const int t = tq * 16 + i;
;                 const float bt = dir == 0 ? (pre + cs[i]) : (total - (pre + cs[i]) + lfv[i]);
;                 const float q = qv[i];
;                 const float key = 1.f - fexp(lfv[i]);
;                 *(LAS bf16_t*)(lds + C3_QT + t * R272 + d * 2) = f2bf(q * fexp(bt));
;                 *(LAS bf16_t*)(lds + C3_QH + t * R272 + d * 2) = f2bf(q * fexp(fminf(bt - mref, 80.f)));
;                 *(LAS bf16_t*)(lds + C3_KH + t * R272 + d * 2) = f2bf(key * fexp(fminf(mref - bt, 80.f)));
;             }
.LBB0_1097:
	s_waitcnt vmcnt(19)
	v_lshlrev_b32_e32 v215, 16, v162
	v_mul_f32_e32 v215, 0x3fb8aa3b, v215
	s_waitcnt vmcnt(18)
	v_lshlrev_b32_e32 v220, 16, v164
	v_mul_f32_e32 v220, 0x3fb8aa3b, v220
	v_add_f32_e32 v224, 0, v215
	s_waitcnt vmcnt(17)
	v_lshlrev_b32_e32 v221, 16, v65
	v_mul_f32_e32 v221, 0x3fb8aa3b, v221
	v_add_f32_e32 v225, v224, v220
	s_waitcnt vmcnt(16)
	v_lshlrev_b32_e32 v222, 16, v166
	v_mul_f32_e32 v222, 0x3fb8aa3b, v222
	v_add_f32_e32 v226, v225, v221
	s_waitcnt vmcnt(15)
	v_lshlrev_b32_e32 v223, 16, v160
	v_mul_f32_e32 v223, 0x3fb8aa3b, v223
	v_add_f32_e32 v227, v226, v222
	s_waitcnt vmcnt(14)
	v_lshlrev_b32_e32 v213, 16, v161
	v_mul_f32_e32 v213, 0x3fb8aa3b, v213
	v_add_f32_e32 v228, v227, v223
	s_waitcnt vmcnt(13)
	v_lshlrev_b32_e32 v211, 16, v163
	v_mul_f32_e32 v211, 0x3fb8aa3b, v211
	v_add_f32_e32 v214, v228, v213
	s_waitcnt vmcnt(12)
	v_lshlrev_b32_e32 v209, 16, v169
	v_mul_f32_e32 v209, 0x3fb8aa3b, v209
	v_add_f32_e32 v212, v214, v211
	s_waitcnt vmcnt(11)
	v_lshlrev_b32_e32 v207, 16, v165
	v_mul_f32_e32 v207, 0x3fb8aa3b, v207
	v_add_f32_e32 v210, v212, v209
	s_waitcnt vmcnt(10)
	v_lshlrev_b32_e32 v51, 16, v167
	v_mul_f32_e32 v51, 0x3fb8aa3b, v51
	v_add_f32_e32 v208, v210, v207
	s_waitcnt vmcnt(9)
	v_lshlrev_b32_e32 v49, 16, v168
	v_mul_f32_e32 v49, 0x3fb8aa3b, v49
	v_add_f32_e32 v206, v208, v51
	s_waitcnt vmcnt(8)
	v_lshlrev_b32_e32 v47, 16, v172
	v_mul_f32_e32 v47, 0x3fb8aa3b, v47
	v_add_f32_e32 v50, v206, v49
	s_waitcnt vmcnt(7)
	v_lshlrev_b32_e32 v45, 16, v170
	v_mul_f32_e32 v45, 0x3fb8aa3b, v45
	v_add_f32_e32 v48, v50, v47
	s_waitcnt vmcnt(6)
	v_lshlrev_b32_e32 v43, 16, v171
	v_mul_f32_e32 v43, 0x3fb8aa3b, v43
	v_add_f32_e32 v46, v48, v45
	s_waitcnt vmcnt(5)
	v_lshlrev_b32_e32 v41, 16, v173
	v_mul_f32_e32 v41, 0x3fb8aa3b, v41
	v_add_f32_e32 v44, v46, v43
	s_waitcnt vmcnt(4)
	v_lshlrev_b32_e32 v37, 16, v174
	v_mul_f32_e32 v37, 0x3fb8aa3b, v37
	v_add_f32_e32 v42, v44, v41
	v_add_f32_e32 v38, v42, v37
	s_waitcnt lgkmcnt(0)
	s_barrier
	ds_write_b32 v175, v38
	s_waitcnt vmcnt(3)
	ds_write_b128 v181, v[2:5]
	s_waitcnt vmcnt(2)
	ds_write_b128 v182, v[6:9]
	s_waitcnt vmcnt(1)
	ds_write_b128 v183, v[10:13]
	s_waitcnt vmcnt(0)
	ds_write_b128 v184, v[14:17]
	s_waitcnt lgkmcnt(0)
	s_barrier
	ds_read2st64_b32 v[216:217], v176 offset1:2
	ds_read2st64_b32 v[218:219], v176 offset0:4 offset1:6
	s_xor_b64 s[78:79], s[2:3], -1
	s_and_b64 vcc, exec, s[78:79]
	s_mov_b64 s[92:93], -1
	s_waitcnt lgkmcnt(1)
	v_cndmask_b32_e64 v36, 0, v216, s[4:5]
	v_cndmask_b32_e64 v39, 0, v217, s[6:7]
	v_add_f32_e32 v36, v36, v39
	s_waitcnt lgkmcnt(0)
	v_cndmask_b32_e64 v39, 0, v218, s[8:9]
	v_add_f32_e32 v39, v36, v39
	v_add_f32_e32 v36, v216, v217
	v_add_f32_e32 v216, v218, v219
	v_add_f32_e32 v40, v36, v216
	v_cndmask_b32_e64 v36, v216, v36, s[2:3]
	v_add_f32_e32 v216, v224, v39
	v_sub_f32_e32 v217, v40, v216
	v_add_f32_e32 v217, v217, v215
	v_cndmask_b32_e64 v216, v217, v216, s[2:3]
	v_exp_f32_e32 v217, v216
	v_exp_f32_e32 v215, v215
	v_add_f32_e32 v214, v214, v39
	v_mul_f32_e32 v217, v217, v190
	v_cvt_pk_bf16_f32 v217, v217, v217
	ds_write_b16 v185, v217
	v_sub_f32_e32 v217, v216, v36
	v_sub_f32_e32 v216, v36, v216
	v_min_f32_e32 v216, 0x42e6d4ca, v216
	v_exp_f32_e32 v216, v216
	v_min_f32_e32 v217, 0x42e6d4ca, v217
	v_sub_f32_e32 v215, 1.0, v215
	v_exp_f32_e32 v217, v217
	v_mul_f32_e32 v215, v215, v216
	v_cvt_pk_bf16_f32 v215, v215, v215
	ds_write_b16 v185, v215 offset:34816
	v_add_f32_e32 v215, v225, v39
	v_mul_f32_e32 v217, v217, v190
	v_sub_f32_e32 v216, v40, v215
	v_add_f32_e32 v216, v216, v220
	v_cvt_pk_bf16_f32 v217, v217, v217
	v_cndmask_b32_e64 v215, v216, v215, s[2:3]
	ds_write_b16 v185, v217 offset:17408
	v_exp_f32_e32 v217, v215
	v_exp_f32_e32 v216, v220
	v_add_f32_e32 v212, v212, v39
	v_mul_f32_e32 v217, v217, v191
	v_cvt_pk_bf16_f32 v217, v217, v217
	ds_write_b16 v185, v217 offset:272
	v_sub_f32_e32 v217, v215, v36
	v_sub_f32_e32 v215, v36, v215
	v_min_f32_e32 v215, 0x42e6d4ca, v215
	v_exp_f32_e32 v215, v215
	v_min_f32_e32 v217, 0x42e6d4ca, v217
	v_sub_f32_e32 v216, 1.0, v216
	v_exp_f32_e32 v217, v217
	v_mul_f32_e32 v215, v216, v215
	v_cvt_pk_bf16_f32 v215, v215, v215
	ds_write_b16 v185, v215 offset:35088
	v_add_f32_e32 v215, v226, v39
	v_mul_f32_e32 v217, v217, v191
	v_sub_f32_e32 v216, v40, v215
	v_add_f32_e32 v216, v216, v221
	v_cvt_pk_bf16_f32 v217, v217, v217
	v_cndmask_b32_e64 v215, v216, v215, s[2:3]
	ds_write_b16 v185, v217 offset:17680
	v_exp_f32_e32 v217, v215
	v_exp_f32_e32 v216, v221
	v_add_f32_e32 v210, v210, v39
	v_mul_f32_e32 v217, v217, v192
	v_cvt_pk_bf16_f32 v217, v217, v217
	ds_write_b16 v185, v217 offset:544
	v_sub_f32_e32 v217, v215, v36
	v_sub_f32_e32 v215, v36, v215
	v_min_f32_e32 v215, 0x42e6d4ca, v215
	v_exp_f32_e32 v215, v215
	v_min_f32_e32 v217, 0x42e6d4ca, v217
	v_sub_f32_e32 v216, 1.0, v216
	v_exp_f32_e32 v217, v217
	v_mul_f32_e32 v215, v216, v215
	v_cvt_pk_bf16_f32 v215, v215, v215
	ds_write_b16 v185, v215 offset:35360
	v_add_f32_e32 v215, v227, v39
	v_mul_f32_e32 v217, v217, v192
	v_sub_f32_e32 v216, v40, v215
	v_add_f32_e32 v216, v216, v222
	v_cvt_pk_bf16_f32 v217, v217, v217
	v_cndmask_b32_e64 v215, v216, v215, s[2:3]
	ds_write_b16 v185, v217 offset:17952
	v_exp_f32_e32 v217, v215
	v_exp_f32_e32 v216, v222
	v_add_f32_e32 v208, v208, v39
	v_mul_f32_e32 v217, v217, v193
	v_cvt_pk_bf16_f32 v217, v217, v217
	ds_write_b16 v185, v217 offset:816
	v_sub_f32_e32 v217, v215, v36
	v_sub_f32_e32 v215, v36, v215
	v_min_f32_e32 v215, 0x42e6d4ca, v215
	v_exp_f32_e32 v215, v215
	v_min_f32_e32 v217, 0x42e6d4ca, v217
	v_sub_f32_e32 v216, 1.0, v216
	v_exp_f32_e32 v217, v217
	v_mul_f32_e32 v215, v216, v215
; #define LAS __attribute__((address_space(3)))
; __device__ __forceinline__ bf16_t f2bf(float f) { unsigned u = __float_as_uint(f); u += 0x7FFFu + ((u >> 16) & 1u); return (bf16_t)(u >> 16); }
; __device__ __forceinline__ float fexp(float x) { return __builtin_amdgcn_exp2f(x * 1.4426950408889634f); }
; #define lds lds_hidden(lds0)
; __device__ __forceinline__ void c3_phase(LAS unsigned char* lds, const bf16_t* __restrict__ QH, const bf16_t* __restrict__ LF, const bf16_t* __restrict__ VTH, const bf16_t* __restrict__ SIN, ...
;     ...
; #pragma unroll
;             for (int i = 0; i < 16; ++i) {
;                 const int t = tq * 16 + i;
;                 const float bt = dir == 0 ? (pre + cs[i]) : (total - (pre + cs[i]) + lfv[i]);
;                 const float q = qv[i];
;                 const float key = 1.f - fexp(lfv[i]);
;                 *(LAS bf16_t*)(lds + C3_QT + t * R272 + d * 2) = f2bf(q * fexp(bt));
;                 *(LAS bf16_t*)(lds + C3_QH + t * R272 + d * 2) = f2bf(q * fexp(fminf(bt - mref, 80.f)));
;                 *(LAS bf16_t*)(lds + C3_KH + t * R272 + d * 2) = f2bf(key * fexp(fminf(mref - bt, 80.f)));
;             }
	v_cvt_pk_bf16_f32 v215, v215, v215
	ds_write_b16 v185, v215 offset:35632
	v_add_f32_e32 v215, v228, v39
	v_mul_f32_e32 v217, v217, v193
	v_sub_f32_e32 v216, v40, v215
	v_add_f32_e32 v216, v216, v223
	v_cvt_pk_bf16_f32 v217, v217, v217
	v_cndmask_b32_e64 v215, v216, v215, s[2:3]
	ds_write_b16 v185, v217 offset:18224
	v_exp_f32_e32 v217, v215
	v_exp_f32_e32 v216, v223
	v_add_f32_e32 v206, v206, v39
	v_mul_f32_e32 v217, v217, v194
	v_cvt_pk_bf16_f32 v217, v217, v217
	ds_write_b16 v185, v217 offset:1088
	v_sub_f32_e32 v217, v215, v36
	v_sub_f32_e32 v215, v36, v215
	v_min_f32_e32 v215, 0x42e6d4ca, v215
	v_exp_f32_e32 v215, v215
	v_sub_f32_e32 v216, 1.0, v216
	v_add_f32_e32 v50, v50, v39
	v_add_f32_e32 v48, v48, v39
	v_mul_f32_e32 v215, v216, v215
	v_cvt_pk_bf16_f32 v215, v215, v215
	ds_write_b16 v185, v215 offset:35904
	v_sub_f32_e32 v215, v40, v214
	v_add_f32_e32 v215, v215, v213
	v_cndmask_b32_e64 v214, v215, v214, s[2:3]
	v_exp_f32_e32 v215, v214
	v_exp_f32_e32 v213, v213
	v_add_f32_e32 v46, v46, v39
	v_mul_f32_e32 v215, v215, v195
	v_cvt_pk_bf16_f32 v215, v215, v215
	ds_write_b16 v185, v215 offset:1360
	v_sub_f32_e32 v215, v214, v36
	v_sub_f32_e32 v214, v36, v214
	v_min_f32_e32 v214, 0x42e6d4ca, v214
	v_exp_f32_e32 v214, v214
	v_sub_f32_e32 v213, 1.0, v213
	v_add_f32_e32 v44, v44, v39
	v_add_f32_e32 v42, v42, v39
	v_mul_f32_e32 v213, v213, v214
	v_cvt_pk_bf16_f32 v213, v213, v213
	ds_write_b16 v185, v213 offset:36176
	v_sub_f32_e32 v213, v40, v212
	v_add_f32_e32 v213, v213, v211
	v_cndmask_b32_e64 v212, v213, v212, s[2:3]
	v_exp_f32_e32 v213, v212
	v_exp_f32_e32 v211, v211
	v_add_f32_e32 v38, v38, v39
	v_mul_f32_e32 v213, v213, v196
	v_cvt_pk_bf16_f32 v213, v213, v213
	ds_write_b16 v185, v213 offset:1632
	v_sub_f32_e32 v213, v212, v36
	v_sub_f32_e32 v212, v36, v212
	v_min_f32_e32 v212, 0x42e6d4ca, v212
	v_exp_f32_e32 v212, v212
	v_sub_f32_e32 v211, 1.0, v211
	v_sub_f32_e32 v39, v40, v38
	v_add_f32_e32 v39, v39, v37
	v_mul_f32_e32 v211, v211, v212
	v_cvt_pk_bf16_f32 v211, v211, v211
	ds_write_b16 v185, v211 offset:36448
	v_sub_f32_e32 v211, v40, v210
	v_add_f32_e32 v211, v211, v209
	v_cndmask_b32_e64 v210, v211, v210, s[2:3]
	v_exp_f32_e32 v211, v210
	v_exp_f32_e32 v209, v209
	v_cndmask_b32_e64 v38, v39, v38, s[2:3]
	v_mul_f32_e32 v211, v211, v197
	v_cvt_pk_bf16_f32 v211, v211, v211
	ds_write_b16 v185, v211 offset:1904
	v_sub_f32_e32 v211, v210, v36
	v_sub_f32_e32 v210, v36, v210
	v_min_f32_e32 v210, 0x42e6d4ca, v210
	v_exp_f32_e32 v210, v210
	v_sub_f32_e32 v209, 1.0, v209
	v_exp_f32_e32 v39, v38
	v_mul_f32_e32 v209, v209, v210
	v_cvt_pk_bf16_f32 v209, v209, v209
	ds_write_b16 v185, v209 offset:36720
	v_sub_f32_e32 v209, v40, v208
	v_add_f32_e32 v209, v209, v207
	v_cndmask_b32_e64 v208, v209, v208, s[2:3]
	v_exp_f32_e32 v209, v208
	v_exp_f32_e32 v207, v207
	v_mul_f32_e32 v39, v39, v205
	v_mul_f32_e32 v209, v209, v198
	v_cvt_pk_bf16_f32 v209, v209, v209
	ds_write_b16 v185, v209 offset:2176
	v_sub_f32_e32 v209, v208, v36
	v_sub_f32_e32 v208, v36, v208
	v_min_f32_e32 v208, 0x42e6d4ca, v208
	v_exp_f32_e32 v208, v208
	v_sub_f32_e32 v207, 1.0, v207
	v_min_f32_e32 v217, 0x42e6d4ca, v217
	v_min_f32_e32 v215, 0x42e6d4ca, v215
	v_mul_f32_e32 v207, v207, v208
	v_cvt_pk_bf16_f32 v207, v207, v207
	ds_write_b16 v185, v207 offset:36992
	v_sub_f32_e32 v207, v40, v206
	v_add_f32_e32 v207, v207, v51
	v_cndmask_b32_e64 v206, v207, v206, s[2:3]
	v_exp_f32_e32 v207, v206
	v_exp_f32_e32 v51, v51
	v_min_f32_e32 v213, 0x42e6d4ca, v213
	v_mul_f32_e32 v207, v207, v199
	v_cvt_pk_bf16_f32 v207, v207, v207
	ds_write_b16 v185, v207 offset:2448
	v_sub_f32_e32 v207, v206, v36
	v_sub_f32_e32 v206, v36, v206
	v_min_f32_e32 v206, 0x42e6d4ca, v206
	v_exp_f32_e32 v206, v206
	v_sub_f32_e32 v51, 1.0, v51
	v_min_f32_e32 v211, 0x42e6d4ca, v211
	v_min_f32_e32 v209, 0x42e6d4ca, v209
	v_mul_f32_e32 v51, v51, v206
	v_cvt_pk_bf16_f32 v51, v51, v51
	ds_write_b16 v185, v51 offset:37264
	v_sub_f32_e32 v51, v40, v50
	v_add_f32_e32 v51, v51, v49
	v_cndmask_b32_e64 v50, v51, v50, s[2:3]
	v_exp_f32_e32 v51, v50
	v_exp_f32_e32 v49, v49
	v_min_f32_e32 v207, 0x42e6d4ca, v207
	v_mul_f32_e32 v51, v51, v200
	v_cvt_pk_bf16_f32 v51, v51, v51
	ds_write_b16 v185, v51 offset:2720
	v_sub_f32_e32 v51, v50, v36
	v_sub_f32_e32 v50, v36, v50
	v_min_f32_e32 v50, 0x42e6d4ca, v50
	v_exp_f32_e32 v50, v50
	v_sub_f32_e32 v49, 1.0, v49
	v_min_f32_e32 v51, 0x42e6d4ca, v51
	v_mul_f32_e32 v49, v49, v50
	v_cvt_pk_bf16_f32 v49, v49, v49
	ds_write_b16 v185, v49 offset:37536
	v_sub_f32_e32 v49, v40, v48
	v_add_f32_e32 v49, v49, v47
	v_cndmask_b32_e64 v48, v49, v48, s[2:3]
	v_exp_f32_e32 v49, v48
	v_exp_f32_e32 v47, v47
	v_mul_f32_e32 v49, v49, v201
	v_cvt_pk_bf16_f32 v49, v49, v49
	ds_write_b16 v185, v49 offset:2992
	v_sub_f32_e32 v49, v48, v36
; #define LAS __attribute__((address_space(3)))
; __device__ __forceinline__ bf16_t f2bf(float f) { unsigned u = __float_as_uint(f); u += 0x7FFFu + ((u >> 16) & 1u); return (bf16_t)(u >> 16); }
; __device__ __forceinline__ float fexp(float x) { return __builtin_amdgcn_exp2f(x * 1.4426950408889634f); }
; #define lds lds_hidden(lds0)
; __device__ __forceinline__ void c3_phase(LAS unsigned char* lds, const bf16_t* __restrict__ QH, const bf16_t* __restrict__ LF, const bf16_t* __restrict__ VTH, const bf16_t* __restrict__ SIN, ...
;     ...
; #pragma unroll
;             for (int i = 0; i < 16; ++i) {
;                 const int t = tq * 16 + i;
;                 const float bt = dir == 0 ? (pre + cs[i]) : (total - (pre + cs[i]) + lfv[i]);
;                 const float q = qv[i];
;                 const float key = 1.f - fexp(lfv[i]);
;                 *(LAS bf16_t*)(lds + C3_QT + t * R272 + d * 2) = f2bf(q * fexp(bt));
;                 *(LAS bf16_t*)(lds + C3_QH + t * R272 + d * 2) = f2bf(q * fexp(fminf(bt - mref, 80.f)));
;                 *(LAS bf16_t*)(lds + C3_KH + t * R272 + d * 2) = f2bf(key * fexp(fminf(mref - bt, 80.f)));
;             }
;             __syncthreads();
;             if (dir == 0) C3_PREFETCH(item, 1); else if (item + G < NB * 4 * 32) C3_PREFETCH(item + G, 0);
	v_sub_f32_e32 v48, v36, v48
	v_min_f32_e32 v48, 0x42e6d4ca, v48
	v_exp_f32_e32 v48, v48
	v_sub_f32_e32 v47, 1.0, v47
	v_min_f32_e32 v49, 0x42e6d4ca, v49
	v_mul_f32_e32 v47, v47, v48
	v_cvt_pk_bf16_f32 v47, v47, v47
	ds_write_b16 v185, v47 offset:37808
	v_sub_f32_e32 v47, v40, v46
	v_add_f32_e32 v47, v47, v45
	v_cndmask_b32_e64 v46, v47, v46, s[2:3]
	v_exp_f32_e32 v47, v46
	v_exp_f32_e32 v45, v45
	v_mul_f32_e32 v47, v47, v202
	v_cvt_pk_bf16_f32 v47, v47, v47
	ds_write_b16 v185, v47 offset:3264
	v_sub_f32_e32 v47, v46, v36
	v_sub_f32_e32 v46, v36, v46
	v_min_f32_e32 v46, 0x42e6d4ca, v46
	v_exp_f32_e32 v46, v46
	v_sub_f32_e32 v45, 1.0, v45
	v_min_f32_e32 v47, 0x42e6d4ca, v47
	v_mul_f32_e32 v45, v45, v46
	v_cvt_pk_bf16_f32 v45, v45, v45
	ds_write_b16 v185, v45 offset:38080
	v_sub_f32_e32 v45, v40, v44
	v_add_f32_e32 v45, v45, v43
	v_cndmask_b32_e64 v44, v45, v44, s[2:3]
	v_exp_f32_e32 v45, v44
	v_exp_f32_e32 v43, v43
	v_mul_f32_e32 v45, v45, v203
	v_cvt_pk_bf16_f32 v45, v45, v45
	ds_write_b16 v185, v45 offset:3536
	v_sub_f32_e32 v45, v44, v36
	v_sub_f32_e32 v44, v36, v44
	v_min_f32_e32 v44, 0x42e6d4ca, v44
	v_exp_f32_e32 v44, v44
	v_sub_f32_e32 v43, 1.0, v43
	v_min_f32_e32 v45, 0x42e6d4ca, v45
	v_mul_f32_e32 v43, v43, v44
	v_cvt_pk_bf16_f32 v43, v43, v43
	ds_write_b16 v185, v43 offset:38352
	v_sub_f32_e32 v43, v40, v42
	v_add_f32_e32 v43, v43, v41
	v_cndmask_b32_e64 v42, v43, v42, s[2:3]
	v_exp_f32_e32 v43, v42
	v_cvt_pk_bf16_f32 v39, v39, v39
	ds_write_b16 v185, v39 offset:4080
	v_mul_f32_e32 v43, v43, v204
	v_cvt_pk_bf16_f32 v43, v43, v43
	ds_write_b16 v185, v43 offset:3808
	v_sub_f32_e32 v43, v42, v36
	v_sub_f32_e32 v42, v36, v42
	v_sub_f32_e32 v39, v38, v36
	v_sub_f32_e32 v36, v36, v38
	v_min_f32_e32 v43, 0x42e6d4ca, v43
	v_min_f32_e32 v42, 0x42e6d4ca, v42
	v_min_f32_e32 v39, 0x42e6d4ca, v39
	v_min_f32_e32 v36, 0x42e6d4ca, v36
	v_exp_f32_e32 v41, v41
	v_exp_f32_e32 v37, v37
	v_exp_f32_e32 v217, v217
	v_exp_f32_e32 v215, v215
	v_exp_f32_e32 v213, v213
	v_exp_f32_e32 v211, v211
	v_exp_f32_e32 v209, v209
	v_exp_f32_e32 v207, v207
	v_exp_f32_e32 v51, v51
	v_exp_f32_e32 v49, v49
	v_exp_f32_e32 v47, v47
	v_exp_f32_e32 v45, v45
	v_exp_f32_e32 v43, v43
	v_exp_f32_e32 v42, v42
	v_exp_f32_e32 v39, v39
	v_exp_f32_e32 v36, v36
	v_sub_f32_e32 v41, 1.0, v41
	v_sub_f32_e32 v37, 1.0, v37
	v_mul_f32_e32 v217, v217, v194
	v_mul_f32_e32 v215, v215, v195
	v_mul_f32_e32 v213, v213, v196
	v_mul_f32_e32 v211, v211, v197
	v_mul_f32_e32 v209, v209, v198
	v_mul_f32_e32 v207, v207, v199
	v_mul_f32_e32 v51, v51, v200
	v_mul_f32_e32 v49, v49, v201
	v_mul_f32_e32 v47, v47, v202
	v_mul_f32_e32 v45, v45, v203
	v_mul_f32_e32 v43, v43, v204
	v_mul_f32_e32 v41, v41, v42
	v_mul_f32_e32 v39, v39, v205
	v_mul_f32_e32 v36, v37, v36
	v_cvt_pk_bf16_f32 v217, v217, v217
	v_cvt_pk_bf16_f32 v215, v215, v215
	v_cvt_pk_bf16_f32 v213, v213, v213
	v_cvt_pk_bf16_f32 v211, v211, v211
	v_cvt_pk_bf16_f32 v209, v209, v209
	v_cvt_pk_bf16_f32 v207, v207, v207
	v_cvt_pk_bf16_f32 v51, v51, v51
	v_cvt_pk_bf16_f32 v49, v49, v49
	v_cvt_pk_bf16_f32 v47, v47, v47
	v_cvt_pk_bf16_f32 v45, v45, v45
	v_cvt_pk_bf16_f32 v43, v43, v43
	v_cvt_pk_bf16_f32 v41, v41, v41
	v_cvt_pk_bf16_f32 v39, v39, v39
	v_cvt_pk_bf16_f32 v36, v36, v36
	ds_write_b16 v185, v217 offset:18496
	ds_write_b16 v185, v215 offset:18768
	ds_write_b16 v185, v213 offset:19040
	ds_write_b16 v185, v211 offset:19312
	ds_write_b16 v185, v209 offset:19584
	ds_write_b16 v185, v207 offset:19856
	ds_write_b16 v185, v51 offset:20128
	ds_write_b16 v185, v49 offset:20400
	ds_write_b16 v185, v47 offset:20672
	ds_write_b16 v185, v45 offset:20944
	ds_write_b16 v185, v43 offset:21216
	ds_write_b16 v185, v41 offset:38624
	ds_write_b16 v185, v39 offset:21488
	ds_write_b16 v185, v36 offset:38896
	s_waitcnt lgkmcnt(0)
	s_barrier
	s_cbranch_vccz .LBB0_1101
	s_andn2_b64 vcc, exec, s[86:87]
	s_cbranch_vccnz .LBB0_1100
	global_load_ushort v162, v[82:83], off
	global_load_ushort v164, v[82:83], off offset:2048
	global_load_ushort v65, v[84:85], off
	global_load_ushort v166, v[86:87], off
	global_load_ushort v160, v[88:89], off
	global_load_ushort v161, v[90:91], off
	global_load_ushort v163, v[92:93], off
	global_load_ushort v169, v[94:95], off
	global_load_ushort v165, v[96:97], off
	global_load_ushort v167, v[98:99], off
	global_load_ushort v168, v[100:101], off
	global_load_ushort v172, v[102:103], off
	global_load_ushort v170, v[104:105], off
	global_load_ushort v171, v[106:107], off
	global_load_ushort v173, v[108:109], off
	global_load_ushort v174, v[110:111], off
	global_load_dwordx4 v[2:5], v[112:113], off nt
	global_load_dwordx4 v[6:9], v[114:115], off nt
	global_load_dwordx4 v[10:13], v[116:117], off nt
	global_load_dwordx4 v[14:17], v[118:119], off nt
